# v102 + P3 attention step: next-tile LDS staging (vmcnt waits + ds_write K/V^T) and tile+2 global loads issued right after the QK MFMAs/V reads instead of after the PV MFMAs before the barrier
# baseline (speedup 1.0000x reference)
; #define LAS __attribute__((address_space(3)))
; __device__ __forceinline__ void attn_phase_mfma(Frame& F) {
;     ...
; #pragma unroll
;                 for (int r = 0; r < 16; ++r) s[r] = 0.f;
;                 bf16x8 kf[8];
; #pragma unroll
;                 for (int ks = 0; ks < 8; ++ks) kf[ks] = *(const LAS bf16x8*)(KB + c * AT_KPITCH + (16 * ks + 8 * hh) * 2);
;                 __builtin_amdgcn_sched_barrier(0);
; #pragma unroll
;                 for (int ks = 0; ks < 8; ++ks) s = __builtin_amdgcn_mfma_f32_32x32x16_bf16(kf[ks], qf[ks], s, 0, 0, 0);
;                 v4u vfr[4][2];
; #pragma unroll
;                 for (int db = 0; db < 4; ++db)
; #pragma unroll
;                     for (int s2 = 0; s2 < 2; ++s2) { const LAS unsigned char* vp = VB + (32 * db + c) * AT_VPITCH + (16 * s2 + 4 * hh) * 2;
;                         const v2u lo = *(const LAS v2u*)vp, hi = *(const LAS v2u*)(vp + 16); vfr[db][s2] = (v4u){lo.x, lo.y, hi.x, hi.y}; }
;                 __builtin_amdgcn_sched_barrier(0);
.LBB0_550:
	s_mul_i32 s0, s18, 0x2200
	v_add_u32_e32 v68, s0, v221
	ds_read_b128 v[64:67], v68
	ds_read_b128 v[80:83], v68 offset:32
	ds_read_b128 v[84:87], v68 offset:64
	ds_read_b128 v[88:91], v68 offset:96
	ds_read_b128 v[92:95], v68 offset:128
	ds_read_b128 v[144:147], v68 offset:160
	ds_read_b128 v[148:151], v68 offset:192
	ds_read_b128 v[152:155], v68 offset:224
	s_waitcnt lgkmcnt(7)
	v_mfma_f32_32x32x16_bf16 v[64:79], v[64:67], v[136:139], 0
	s_mul_i32 s0, s18, 0x2400
	s_waitcnt lgkmcnt(6)
	v_mfma_f32_32x32x16_bf16 v[64:79], v[80:83], v[112:115], v[64:79]
	v_add_u32_e32 v80, s0, v226
	v_add_u32_e32 v81, 0x8800, v80
	s_waitcnt lgkmcnt(5)
	v_mfma_f32_32x32x16_bf16 v[64:79], v[84:87], v[116:119], v[64:79]
	s_waitcnt lgkmcnt(4)
	v_mfma_f32_32x32x16_bf16 v[64:79], v[88:91], v[120:123], v[64:79]
	s_waitcnt lgkmcnt(3)
	v_mfma_f32_32x32x16_bf16 v[64:79], v[92:95], v[124:127], v[64:79]
	s_waitcnt lgkmcnt(2)
	v_mfma_f32_32x32x16_bf16 v[64:79], v[144:147], v[128:131], v[64:79]
	s_waitcnt lgkmcnt(1)
	v_mfma_f32_32x32x16_bf16 v[64:79], v[148:151], v[132:135], v[64:79]
	ds_read2_b64 v[148:151], v81 offset1:2
	ds_read2_b64 v[144:147], v81 offset0:4 offset1:6
	v_add_u32_e32 v81, 0x9000, v80
	s_waitcnt lgkmcnt(2)
	v_mfma_f32_32x32x16_bf16 v[64:79], v[152:155], v[140:143], v[64:79]
	ds_read2_b64 v[152:155], v81 offset0:32 offset1:34
	ds_read2_b64 v[156:159], v81 offset0:36 offset1:38
	v_add_u32_e32 v81, 0x9800, v80
	v_add_u32_e32 v80, 0xa000, v80
	ds_read2_b64 v[164:167], v81 offset0:64 offset1:66
	ds_read2_b64 v[168:171], v81 offset0:68 offset1:70
	ds_read2_b64 v[172:175], v80 offset0:96 offset1:98
	ds_read2_b64 v[160:163], v80 offset0:100 offset1:102
	v_lshrrev_b32_e32 v233, v222, v229
	v_and_b32_e32 v199, 1, v233
	v_and_b32_e32 v198, 2, v233
	v_and_b32_e32 v242, 4, v233
	v_and_b32_e32 v250, 8, v233
	v_and_b32_e32 v249, 0x100, v233
	v_and_b32_e32 v248, 0x200, v233
	v_and_b32_e32 v244, 0x400, v233
	v_and_b32_e32 v243, 0x800, v233
	v_and_b32_e32 v241, 0x10000, v233
	v_and_b32_e32 v240, 0x20000, v233
	v_and_b32_e32 v239, 0x40000, v233
	v_and_b32_e32 v238, 0x80000, v233
	v_and_b32_e32 v237, 0x1000000, v233
	v_and_b32_e32 v236, 0x2000000, v233
	v_and_b32_e32 v235, 0x4000000, v233
	s_cmp_gt_i32 s15, s12
	s_cbranch_scc1 .Lp3e_nowrite
	s_xor_b32 s36, s18, 1
	s_mul_i32 s37, s36, 0x2200
	s_mulk_i32 s36, 0x2400
	v_add_u32_e32 v82, s37, v224
	s_waitcnt vmcnt(3)
	ds_write_b128 v82, v[96:99]
	s_waitcnt vmcnt(2)
	ds_write_b128 v82, v[100:103] offset:4352
	s_waitcnt vmcnt(1)
	v_and_b32_e32 v82, 0xffff, v104
	v_add_u32_e32 v83, s36, v225
	v_lshrrev_b32_e32 v84, 16, v104
	s_waitcnt vmcnt(0)
	v_lshl_or_b32 v82, v108, 16, v82
	v_and_or_b32 v84, v108, s92, v84
	v_add_u32_e32 v83, 0x8800, v83
	ds_write2_b32 v83, v82, v84 offset1:18
	v_and_b32_e32 v82, 0xffff, v105
	v_lshrrev_b32_e32 v84, 16, v105
	v_lshl_or_b32 v82, v109, 16, v82
	v_and_or_b32 v84, v109, s92, v84
	ds_write2_b32 v83, v82, v84 offset0:36 offset1:54
	v_and_b32_e32 v82, 0xffff, v106
	v_lshrrev_b32_e32 v84, 16, v106
	v_lshl_or_b32 v82, v110, 16, v82
	v_and_or_b32 v84, v110, s92, v84
	ds_write2_b32 v83, v82, v84 offset0:72 offset1:90
	v_and_b32_e32 v82, 0xffff, v107
	v_lshrrev_b32_e32 v84, 16, v107
	v_lshl_or_b32 v82, v111, 16, v82
	v_and_or_b32 v84, v111, s92, v84
	v_mov_b32_e32 v229, v230
	ds_write2_b32 v83, v82, v84 offset0:108 offset1:126
.Lp3e_nowrite:
	s_add_i32 s36, s15, 4
	s_cmp_gt_u32 s36, s10
	s_cbranch_scc1 .Lp3e_noload
	v_lshl_add_u64 v[82:83], s[26:27], 0, v[212:213]
	global_load_dword v230, v[82:83], off
	v_lshl_add_u64 v[82:83], s[26:27], 0, v[214:215]
	v_lshl_add_u64 v[84:85], s[26:27], 0, v[216:217]
	global_load_dwordx4 v[96:99], v[82:83], off
	global_load_dwordx4 v[100:103], v[84:85], off
	v_lshl_add_u64 v[82:83], s[26:27], 0, v[218:219]
	v_add_co_u32_e32 v84, vcc, 0xa902000, v82
	s_nop 1
	v_addc_co_u32_e32 v85, vcc, 0, v83, vcc
	v_add_co_u32_e32 v82, vcc, 0xa906000, v82
	s_nop 1
	v_addc_co_u32_e32 v83, vcc, 0, v83, vcc
	global_load_dwordx4 v[104:107], v[84:85], off offset:2560
	global_load_dwordx4 v[108:111], v[82:83], off
.Lp3e_noload:
	s_cmp_lt_i32 s16, s11
	s_mov_b64 s[4:5], -1
	v_cmp_eq_u32_e64 s[60:61], 1, v199
	v_cmp_ne_u32_e64 s[58:59], 0, v198
	v_cmp_ne_u32_e64 s[56:57], 0, v242
	v_cmp_ne_u32_e64 s[54:55], 0, v250
	v_cmp_ne_u32_e64 s[52:53], 0, v249
	v_cmp_ne_u32_e64 s[50:51], 0, v248
	v_cmp_ne_u32_e64 s[48:49], 0, v244
	v_cmp_ne_u32_e64 s[46:47], 0, v243
	v_cmp_ne_u32_e64 s[44:45], 0, v241
	v_cmp_ne_u32_e64 s[42:43], 0, v240
	v_cmp_ne_u32_e64 s[40:41], 0, v239
	v_cmp_ne_u32_e64 s[38:39], 0, v238
	v_cmp_ne_u32_e64 s[36:37], 0, v237
	v_cmp_ne_u32_e64 s[2:3], 0, v236
	v_cmp_ne_u32_e32 vcc, 0, v235
	s_cbranch_scc0 .LBB0_561
	s_andn2_b64 vcc, exec, s[4:5]
	s_cbranch_vccz .LBB0_562

; __device__ __forceinline__ unsigned cvt_pk_bf16(float lo, float hi) { const f32x2 v = {lo, hi}; return __builtin_bit_cast(unsigned, __builtin_convertvector(v, bf16x2_t)); }
; __device__ __forceinline__ void attn_phase_mfma(Frame& F) {
;     ...
;                 bf16x8 pf[2];
; #pragma unroll
;                 for (int s2 = 0; s2 < 2; ++s2) { v4u w; w.x = pg8::cvt_pk_bf16(s[8 * s2 + 0], s[8 * s2 + 1]); w.y = pg8::cvt_pk_bf16(s[8 * s2 + 2], s[8 * s2 + 3]); w.z = pg8::cvt_pk_bf16(s[8 * s2 + 4], s[8 * s2 + 5]); w.w = pg8::cvt_pk_bf16(s[8 * s2 + 6], s[8 * s2 + 7]); pf[s2] = __builtin_bit_cast(bf16x8, w); }
; #pragma unroll
;                 for (int db = 0; db < 4; ++db)
; #pragma unroll
;                     for (int s2 = 0; s2 < 2; ++s2) o[db] = __builtin_amdgcn_mfma_f32_32x32x16_bf16(__builtin_bit_cast(bf16x8, vfr[db][s2]), pf[s2], o[db], 0, 0, 0);
;             }
;             if (kt + 2 <= qb) { AT_WRITE_TILE((st + 1) & 1); mw = mwn; }
.LBB0_554:
	v_cvt_pk_bf16_f32 v64, v80, v81
	v_cvt_pk_bf16_f32 v65, v82, v83
	v_cvt_pk_bf16_f32 v66, v84, v85
	v_cvt_pk_bf16_f32 v67, v86, v87
	v_exp_f32_e32 v68, v95
	v_and_b32_e32 v69, 0x8000000, v233
	s_waitcnt lgkmcnt(7)
	v_mfma_f32_32x32x16_bf16 v[48:63], v[148:151], v[64:67], v[48:63]
	v_cmp_ne_u32_e32 vcc, 0, v69
	v_cvt_pk_bf16_f32 v69, v90, v91
	v_cvt_pk_bf16_f32 v70, v92, v93
	v_cndmask_b32_e32 v72, 0, v68, vcc
	v_cvt_pk_bf16_f32 v68, v88, v89
	v_cvt_pk_bf16_f32 v71, v94, v72
	s_waitcnt lgkmcnt(5)
	v_mfma_f32_32x32x16_bf16 v[32:47], v[152:155], v[64:67], v[32:47]
	s_waitcnt lgkmcnt(3)
	v_mfma_f32_32x32x16_bf16 v[16:31], v[164:167], v[64:67], v[16:31]
	s_waitcnt lgkmcnt(1)
	v_mfma_f32_32x32x16_bf16 v[0:15], v[172:175], v[64:67], v[0:15]
	v_add_f32_e32 v64, v247, v72
	v_add_f32_e32 v210, v64, v210
	v_mfma_f32_32x32x16_bf16 v[48:63], v[144:147], v[68:71], v[48:63]
	v_mfma_f32_32x32x16_bf16 v[32:47], v[156:159], v[68:71], v[32:47]
	v_mfma_f32_32x32x16_bf16 v[16:31], v[168:171], v[68:71], v[16:31]
	s_waitcnt lgkmcnt(0)
	v_mfma_f32_32x32x16_bf16 v[0:15], v[160:163], v[68:71], v[0:15]
	s_branch .LBB0_559
